# P1/P4 bf16 loops: first 3 SP2 DMA stage issues before the LDS reads, last 3 moved into the following MFMA block; SP2 wait vmcnt(5+k)
# speedup vs baseline: 1.0165x; 1.0165x over previous
.Lp1vg_mmafter_b:
	s_barrier
	s_add_u32 s4, s56, 0x80080
	s_addc_u32 s5, s57, 0
	s_mov_b32 m0, s69
	v_lshl_add_u64 v[4:5], v[4:5], 0, s[24:25]
	global_load_lds_dwordx4 v[4:5], off
	v_lshl_add_u64 v[4:5], v[226:227], 0, s[24:25]
	s_mov_b32 m0, s70
	s_nop 0
	global_load_lds_dwordx4 v[4:5], off
	v_lshl_add_u64 v[4:5], s[4:5], 0, v[212:213]
	s_mov_b32 m0, s73
	s_nop 0
	global_load_lds_dwordx4 v[4:5], off
	ds_read_b128 v[174:177], v234 offset:49152
	ds_read_b128 v[178:181], v234 offset:50176
	ds_read_b128 v[182:185], v234 offset:51200
	ds_read_b128 v[186:189], v234 offset:52224
	ds_read_b128 v[190:193], v234 offset:53248
	ds_read_b128 v[194:197], v234 offset:54272
	ds_read_b128 v[198:201], v234 offset:55296
	ds_read_b128 v[202:205], v234 offset:56320
	s_cmp_eq_u32 s100, 3
	s_cbranch_scc1 .Lp1vg_w11_b2
	s_cmp_eq_u32 s100, 2
	s_cbranch_scc1 .Lp1vg_wk2_b2
	s_waitcnt vmcnt(5)
	s_branch .Lp1vg_wd_b2
.Lp1vg_wk2_b2:
	s_waitcnt vmcnt(7)
	s_branch .Lp1vg_wd_b2

.Lp1vg_wd_b2:
	s_waitcnt lgkmcnt(0)
	s_barrier
	s_setprio 1
	s_waitcnt lgkmcnt(0)
	v_mfma_f32_16x16x32_bf16 v[74:77], v[158:161], v[174:177], v[74:77]
	v_mfma_f32_16x16x32_bf16 v[70:73], v[166:169], v[174:177], v[70:73]
	v_lshl_add_u64 v[4:5], s[4:5], 0, v[216:217]
	s_mov_b32 m0, s75
	s_nop 0
	global_load_lds_dwordx4 v[4:5], off
	v_mfma_f32_16x16x32_bf16 v[58:61], v[158:161], v[182:185], v[58:61]
	v_mfma_f32_16x16x32_bf16 v[54:57], v[166:169], v[182:185], v[54:57]
	v_mfma_f32_16x16x32_bf16 v[42:45], v[158:161], v[190:193], v[42:45]
	v_mfma_f32_16x16x32_bf16 v[38:41], v[166:169], v[190:193], v[38:41]
	v_lshl_add_u64 v[4:5], v[228:229], 0, s[24:25]
	s_mov_b32 m0, s71
	s_nop 0
	global_load_lds_dwordx4 v[4:5], off
	v_mfma_f32_16x16x32_bf16 v[26:29], v[158:161], v[198:201], v[26:29]
	v_mfma_f32_16x16x32_bf16 v[22:25], v[166:169], v[198:201], v[22:25]
	v_mfma_f32_16x16x32_bf16 v[74:77], v[162:165], v[178:181], v[74:77]
	v_mfma_f32_16x16x32_bf16 v[70:73], v[170:173], v[178:181], v[70:73]
	v_lshl_add_u64 v[4:5], v[230:231], 0, s[24:25]
	s_mov_b32 m0, s72
	s_nop 0
	global_load_lds_dwordx4 v[4:5], off
	v_mfma_f32_16x16x32_bf16 v[58:61], v[162:165], v[186:189], v[58:61]
	v_mfma_f32_16x16x32_bf16 v[54:57], v[170:173], v[186:189], v[54:57]
	v_mfma_f32_16x16x32_bf16 v[42:45], v[162:165], v[194:197], v[42:45]
	v_mfma_f32_16x16x32_bf16 v[38:41], v[170:173], v[194:197], v[38:41]
	v_mfma_f32_16x16x32_bf16 v[26:29], v[162:165], v[202:205], v[26:29]
	v_mfma_f32_16x16x32_bf16 v[22:25], v[170:173], v[202:205], v[22:25]
	s_setprio 0
	s_setprio 1
	v_mfma_f32_16x16x32_bf16 v[66:69], v[142:145], v[174:177], v[66:69]
	v_mfma_f32_16x16x32_bf16 v[62:65], v[150:153], v[174:177], v[62:65]
	v_mfma_f32_16x16x32_bf16 v[50:53], v[142:145], v[182:185], v[50:53]
	v_mfma_f32_16x16x32_bf16 v[46:49], v[150:153], v[182:185], v[46:49]
	v_mfma_f32_16x16x32_bf16 v[34:37], v[142:145], v[190:193], v[34:37]
	v_mfma_f32_16x16x32_bf16 v[30:33], v[150:153], v[190:193], v[30:33]
	v_mfma_f32_16x16x32_bf16 v[18:21], v[142:145], v[198:201], v[18:21]
	v_mfma_f32_16x16x32_bf16 v[14:17], v[150:153], v[198:201], v[14:17]
	v_mfma_f32_16x16x32_bf16 v[66:69], v[146:149], v[178:181], v[66:69]
	v_mfma_f32_16x16x32_bf16 v[62:65], v[154:157], v[178:181], v[62:65]
	v_mfma_f32_16x16x32_bf16 v[50:53], v[146:149], v[186:189], v[50:53]
	v_mfma_f32_16x16x32_bf16 v[46:49], v[154:157], v[186:189], v[46:49]
	v_mfma_f32_16x16x32_bf16 v[34:37], v[146:149], v[194:197], v[34:37]
	v_mfma_f32_16x16x32_bf16 v[30:33], v[154:157], v[194:197], v[30:33]
	v_mfma_f32_16x16x32_bf16 v[18:21], v[146:149], v[202:205], v[18:21]
	v_mfma_f32_16x16x32_bf16 v[14:17], v[154:157], v[202:205], v[14:17]
	s_setprio 0
	s_barrier
	s_add_i32 s81, s81, 2
	s_add_u32 s54, s54, 0x100
	s_addc_u32 s55, s55, 0
	s_add_u32 s79, s79, 0x100
	s_addc_u32 s80, s80, 0
	s_cmp_gt_u32 s81, 29
	s_cbranch_scc1 .LBB0_180

.Lp1vg_mmjoin_a:
	s_barrier
	s_add_u32 s82, s56, 0x80000
	s_addc_u32 s83, s57, 0
	s_mov_b32 m0, s53
	v_lshl_add_u64 v[4:5], s[56:57], 0, v[212:213]
	global_load_lds_dwordx4 v[4:5], off
	v_lshl_add_u64 v[226:227], s[56:57], 0, v[216:217]
	s_mov_b32 m0, s60
	s_nop 0
	global_load_lds_dwordx4 v[226:227], off
	v_lshl_add_u64 v[228:229], s[82:83], 0, v[212:213]
	s_mov_b32 m0, s61
	v_lshl_add_u64 v[230:231], s[4:5], 0, v[214:215]
	global_load_lds_dwordx4 v[228:229], off
	ds_read_b128 v[174:177], v234 offset:16384
	ds_read_b128 v[178:181], v234 offset:17408
	ds_read_b128 v[182:185], v234 offset:18432
	ds_read_b128 v[186:189], v234 offset:19456
	ds_read_b128 v[190:193], v234 offset:20480
	ds_read_b128 v[194:197], v234 offset:21504
	ds_read_b128 v[198:201], v234 offset:22528
	ds_read_b128 v[202:205], v234 offset:23552
	s_cmp_eq_u32 s100, 3
	s_cbranch_scc1 .Lp1vg_w11_a2
	s_cmp_eq_u32 s100, 2
	s_cbranch_scc1 .Lp1vg_wk2_a2
	s_waitcnt vmcnt(5)
	s_branch .Lp1vg_wd_a2

.Lp1vg_wd_a2:
	s_waitcnt lgkmcnt(0)
	s_barrier
	s_setprio 1
	s_waitcnt lgkmcnt(0)
	v_mfma_f32_16x16x32_bf16 v[74:77], v[158:161], v[174:177], v[74:77]
	v_mfma_f32_16x16x32_bf16 v[70:73], v[166:169], v[174:177], v[70:73]
	v_lshl_add_u64 v[228:229], s[82:83], 0, v[216:217]
	s_mov_b32 m0, s64
	s_nop 0
	global_load_lds_dwordx4 v[228:229], off
	v_mfma_f32_16x16x32_bf16 v[58:61], v[158:161], v[182:185], v[58:61]
	v_mfma_f32_16x16x32_bf16 v[54:57], v[166:169], v[182:185], v[54:57]
	v_mfma_f32_16x16x32_bf16 v[42:45], v[158:161], v[190:193], v[42:45]
	v_mfma_f32_16x16x32_bf16 v[38:41], v[166:169], v[190:193], v[38:41]
	v_lshl_add_u64 v[228:229], s[4:5], 0, v[210:211]
	s_mov_b32 m0, s41
	s_nop 0
	global_load_lds_dwordx4 v[228:229], off
	v_mfma_f32_16x16x32_bf16 v[26:29], v[158:161], v[198:201], v[26:29]
	v_mfma_f32_16x16x32_bf16 v[22:25], v[166:169], v[198:201], v[22:25]
	v_mfma_f32_16x16x32_bf16 v[74:77], v[162:165], v[178:181], v[74:77]
	v_mfma_f32_16x16x32_bf16 v[70:73], v[170:173], v[178:181], v[70:73]
	s_mov_b32 m0, s65
	s_nop 0
	global_load_lds_dwordx4 v[230:231], off
	v_mfma_f32_16x16x32_bf16 v[58:61], v[162:165], v[186:189], v[58:61]
	v_mfma_f32_16x16x32_bf16 v[54:57], v[170:173], v[186:189], v[54:57]
	v_mfma_f32_16x16x32_bf16 v[42:45], v[162:165], v[194:197], v[42:45]
	v_mfma_f32_16x16x32_bf16 v[38:41], v[170:173], v[194:197], v[38:41]
	v_mfma_f32_16x16x32_bf16 v[26:29], v[162:165], v[202:205], v[26:29]
	v_mfma_f32_16x16x32_bf16 v[22:25], v[170:173], v[202:205], v[22:25]
	s_setprio 0
	s_setprio 1
	v_mfma_f32_16x16x32_bf16 v[66:69], v[142:145], v[174:177], v[66:69]
	v_mfma_f32_16x16x32_bf16 v[62:65], v[150:153], v[174:177], v[62:65]
	v_mfma_f32_16x16x32_bf16 v[50:53], v[142:145], v[182:185], v[50:53]
	v_mfma_f32_16x16x32_bf16 v[46:49], v[150:153], v[182:185], v[46:49]
	v_mfma_f32_16x16x32_bf16 v[34:37], v[142:145], v[190:193], v[34:37]
	v_mfma_f32_16x16x32_bf16 v[30:33], v[150:153], v[190:193], v[30:33]
	v_mfma_f32_16x16x32_bf16 v[18:21], v[142:145], v[198:201], v[18:21]
	v_mfma_f32_16x16x32_bf16 v[14:17], v[150:153], v[198:201], v[14:17]
	v_mfma_f32_16x16x32_bf16 v[66:69], v[146:149], v[178:181], v[66:69]
	v_mfma_f32_16x16x32_bf16 v[62:65], v[154:157], v[178:181], v[62:65]
	v_mfma_f32_16x16x32_bf16 v[50:53], v[146:149], v[186:189], v[50:53]
	v_mfma_f32_16x16x32_bf16 v[46:49], v[154:157], v[186:189], v[46:49]
	v_mfma_f32_16x16x32_bf16 v[34:37], v[146:149], v[194:197], v[34:37]
	v_mfma_f32_16x16x32_bf16 v[30:33], v[154:157], v[194:197], v[30:33]
	v_mfma_f32_16x16x32_bf16 v[18:21], v[146:149], v[202:205], v[18:21]
	v_mfma_f32_16x16x32_bf16 v[14:17], v[154:157], v[202:205], v[14:17]
	s_setprio 0
	s_barrier
	v_add_u32_e32 v2, 0x18000, v209
	ds_read_b128 v[158:161], v2
	ds_read_b128 v[162:165], v2 offset:1024
	ds_read_b128 v[166:169], v2 offset:2048
	ds_read_b128 v[170:173], v2 offset:3072
	v_add_u32_e32 v2, 0x1c000, v209
	ds_read_b128 v[142:145], v2
	ds_read_b128 v[146:149], v2 offset:1024
	ds_read_b128 v[150:153], v2 offset:2048
	ds_read_b128 v[154:157], v2 offset:3072
	s_add_u32 s4, s4, 0x80000
	s_addc_u32 s5, s5, 0
	s_mov_b32 m0, s66
	v_lshl_add_u64 v[238:239], s[4:5], 0, v[210:211]
	ds_read_b128 v[198:201], v234 offset:32768
	ds_read_b128 v[202:205], v234 offset:33792
	ds_read_b128 v[190:193], v234 offset:34816
	ds_read_b128 v[194:197], v234 offset:35840
	ds_read_b128 v[182:185], v234 offset:36864
	ds_read_b128 v[186:189], v234 offset:37888
	ds_read_b128 v[174:177], v234 offset:38912
	ds_read_b128 v[178:181], v234 offset:39936
	global_load_lds_dwordx4 v[238:239], off
	v_lshl_add_u64 v[238:239], s[4:5], 0, v[214:215]
	s_mov_b32 m0, s67
	s_nop 0
	global_load_lds_dwordx4 v[238:239], off
	s_cmp_eq_u32 s100, 3
	s_cbranch_scc1 .Lp1vg_w11_b1
	s_cmp_eq_u32 s100, 2
	s_cbranch_scc1 .Lp1vg_wk2_b1
	s_waitcnt vmcnt(8)
	s_branch .Lp1vg_wd_b1

.Lp4vg_mmafter_b:
	s_barrier
	s_add_u32 s4, s34, 0x80080
	s_addc_u32 s5, s35, 0
	s_mov_b32 m0, s48
	v_lshl_add_u64 v[4:5], v[4:5], 0, s[0:1]
	global_load_lds_dwordx4 v[4:5], off
	v_lshl_add_u64 v[4:5], v[222:223], 0, s[0:1]
	s_mov_b32 m0, s49
	s_nop 0
	global_load_lds_dwordx4 v[4:5], off
	v_lshl_add_u64 v[4:5], s[4:5], 0, v[210:211]
	s_mov_b32 m0, s52
	s_nop 0
	global_load_lds_dwordx4 v[4:5], off
	ds_read_b128 v[174:177], v230 offset:49152
	ds_read_b128 v[178:181], v230 offset:50176
	ds_read_b128 v[182:185], v230 offset:51200
	ds_read_b128 v[186:189], v230 offset:52224
	ds_read_b128 v[190:193], v230 offset:53248
	ds_read_b128 v[194:197], v230 offset:54272
	ds_read_b128 v[198:201], v230 offset:55296
	ds_read_b128 v[202:205], v230 offset:56320
	s_cmp_eq_u32 s100, 3
	s_cbranch_scc1 .Lp4vg_w11_b2
	s_cmp_eq_u32 s100, 2
	s_cbranch_scc1 .Lp4vg_wk2_b2
	s_waitcnt vmcnt(5)
	s_branch .Lp4vg_wd_b2

.Lp4vg_wd_b2:
	s_waitcnt lgkmcnt(0)
	s_barrier
	s_setprio 1
	s_waitcnt lgkmcnt(0)
	v_mfma_f32_16x16x32_bf16 v[74:77], v[158:161], v[174:177], v[74:77]
	v_mfma_f32_16x16x32_bf16 v[70:73], v[166:169], v[174:177], v[70:73]
	v_lshl_add_u64 v[4:5], s[4:5], 0, v[212:213]
	s_mov_b32 m0, s53
	s_nop 0
	global_load_lds_dwordx4 v[4:5], off
	v_mfma_f32_16x16x32_bf16 v[62:65], v[158:161], v[182:185], v[62:65]
	v_mfma_f32_16x16x32_bf16 v[58:61], v[166:169], v[182:185], v[58:61]
	v_mfma_f32_16x16x32_bf16 v[46:49], v[158:161], v[190:193], v[46:49]
	v_mfma_f32_16x16x32_bf16 v[42:45], v[166:169], v[190:193], v[42:45]
	v_lshl_add_u64 v[4:5], v[224:225], 0, s[0:1]
	s_mov_b32 m0, s50
	s_nop 0
	global_load_lds_dwordx4 v[4:5], off
	v_mfma_f32_16x16x32_bf16 v[30:33], v[158:161], v[198:201], v[30:33]
	v_mfma_f32_16x16x32_bf16 v[26:29], v[166:169], v[198:201], v[26:29]
	v_mfma_f32_16x16x32_bf16 v[74:77], v[162:165], v[178:181], v[74:77]
	v_mfma_f32_16x16x32_bf16 v[70:73], v[170:173], v[178:181], v[70:73]
	v_lshl_add_u64 v[4:5], v[226:227], 0, s[0:1]
	s_mov_b32 m0, s51
	s_nop 0
	global_load_lds_dwordx4 v[4:5], off
	v_mfma_f32_16x16x32_bf16 v[62:65], v[162:165], v[186:189], v[62:65]
	v_mfma_f32_16x16x32_bf16 v[58:61], v[170:173], v[186:189], v[58:61]
	v_mfma_f32_16x16x32_bf16 v[46:49], v[162:165], v[194:197], v[46:49]
	v_mfma_f32_16x16x32_bf16 v[42:45], v[170:173], v[194:197], v[42:45]
	v_mfma_f32_16x16x32_bf16 v[30:33], v[162:165], v[202:205], v[30:33]
	v_mfma_f32_16x16x32_bf16 v[26:29], v[170:173], v[202:205], v[26:29]
	s_setprio 0
	s_setprio 1
	v_mfma_f32_16x16x32_bf16 v[66:69], v[142:145], v[174:177], v[66:69]
	v_mfma_f32_16x16x32_bf16 v[54:57], v[150:153], v[174:177], v[54:57]
	v_mfma_f32_16x16x32_bf16 v[50:53], v[142:145], v[182:185], v[50:53]
	v_mfma_f32_16x16x32_bf16 v[38:41], v[150:153], v[182:185], v[38:41]
	v_mfma_f32_16x16x32_bf16 v[34:37], v[142:145], v[190:193], v[34:37]
	v_mfma_f32_16x16x32_bf16 v[22:25], v[150:153], v[190:193], v[22:25]
	v_mfma_f32_16x16x32_bf16 v[18:21], v[142:145], v[198:201], v[18:21]
	v_mfma_f32_16x16x32_bf16 v[14:17], v[150:153], v[198:201], v[14:17]
	v_mfma_f32_16x16x32_bf16 v[66:69], v[146:149], v[178:181], v[66:69]
	v_mfma_f32_16x16x32_bf16 v[54:57], v[154:157], v[178:181], v[54:57]
	v_mfma_f32_16x16x32_bf16 v[50:53], v[146:149], v[186:189], v[50:53]
	v_mfma_f32_16x16x32_bf16 v[38:41], v[154:157], v[186:189], v[38:41]
	v_mfma_f32_16x16x32_bf16 v[34:37], v[146:149], v[194:197], v[34:37]
	v_mfma_f32_16x16x32_bf16 v[22:25], v[154:157], v[194:197], v[22:25]
	v_mfma_f32_16x16x32_bf16 v[18:21], v[146:149], v[202:205], v[18:21]
	v_mfma_f32_16x16x32_bf16 v[14:17], v[154:157], v[202:205], v[14:17]
	s_setprio 0
	s_barrier
	s_add_i32 s60, s60, 2
	s_add_u32 s24, s24, 0x100
	s_addc_u32 s25, s25, 0
	s_add_u32 s58, s58, 0x100
	s_addc_u32 s59, s59, 0
	s_cmp_gt_u32 s60, 29
	s_cbranch_scc1 .LBB0_548

.Lp4vg_mmjoin_a:
	s_barrier
	s_add_u32 s64, s34, 0x80000
	s_addc_u32 s65, s35, 0
	s_mov_b32 m0, s33
	v_lshl_add_u64 v[4:5], s[34:35], 0, v[210:211]
	global_load_lds_dwordx4 v[4:5], off
	v_lshl_add_u64 v[222:223], s[34:35], 0, v[212:213]
	s_mov_b32 m0, s36
	s_nop 0
	global_load_lds_dwordx4 v[222:223], off
	v_lshl_add_u64 v[224:225], s[64:65], 0, v[210:211]
	s_mov_b32 m0, s37
	v_lshl_add_u64 v[226:227], s[4:5], 0, v[212:213]
	global_load_lds_dwordx4 v[224:225], off
	ds_read_b128 v[174:177], v230 offset:16384
	ds_read_b128 v[178:181], v230 offset:17408
	ds_read_b128 v[182:185], v230 offset:18432
	ds_read_b128 v[186:189], v230 offset:19456
	ds_read_b128 v[190:193], v230 offset:20480
	ds_read_b128 v[194:197], v230 offset:21504
	ds_read_b128 v[198:201], v230 offset:22528
	ds_read_b128 v[202:205], v230 offset:23552
	s_cmp_eq_u32 s100, 3
	s_cbranch_scc1 .Lp4vg_w11_a2
	s_cmp_eq_u32 s100, 2
	s_cbranch_scc1 .Lp4vg_wk2_a2
	s_waitcnt vmcnt(5)
	s_branch .Lp4vg_wd_a2

.Lp4vg_wd_a2:
	s_waitcnt lgkmcnt(0)
	s_barrier
	s_setprio 1
	s_waitcnt lgkmcnt(0)
	v_mfma_f32_16x16x32_bf16 v[74:77], v[158:161], v[174:177], v[74:77]
	v_mfma_f32_16x16x32_bf16 v[70:73], v[166:169], v[174:177], v[70:73]
	v_lshl_add_u64 v[224:225], s[64:65], 0, v[212:213]
	s_mov_b32 m0, s41
	s_nop 0
	global_load_lds_dwordx4 v[224:225], off
	v_mfma_f32_16x16x32_bf16 v[62:65], v[158:161], v[182:185], v[62:65]
	v_mfma_f32_16x16x32_bf16 v[58:61], v[166:169], v[182:185], v[58:61]
	v_mfma_f32_16x16x32_bf16 v[46:49], v[158:161], v[190:193], v[46:49]
	v_mfma_f32_16x16x32_bf16 v[42:45], v[166:169], v[190:193], v[42:45]
	v_lshl_add_u64 v[224:225], s[4:5], 0, v[210:211]
	s_mov_b32 m0, s21
	s_nop 0
	global_load_lds_dwordx4 v[224:225], off
	v_mfma_f32_16x16x32_bf16 v[30:33], v[158:161], v[198:201], v[30:33]
	v_mfma_f32_16x16x32_bf16 v[26:29], v[166:169], v[198:201], v[26:29]
	v_mfma_f32_16x16x32_bf16 v[74:77], v[162:165], v[178:181], v[74:77]
	v_mfma_f32_16x16x32_bf16 v[70:73], v[170:173], v[178:181], v[70:73]
	s_mov_b32 m0, s43
	s_nop 0
	global_load_lds_dwordx4 v[226:227], off
	v_mfma_f32_16x16x32_bf16 v[62:65], v[162:165], v[186:189], v[62:65]
	v_mfma_f32_16x16x32_bf16 v[58:61], v[170:173], v[186:189], v[58:61]
	v_mfma_f32_16x16x32_bf16 v[46:49], v[162:165], v[194:197], v[46:49]
	v_mfma_f32_16x16x32_bf16 v[42:45], v[170:173], v[194:197], v[42:45]
	v_mfma_f32_16x16x32_bf16 v[30:33], v[162:165], v[202:205], v[30:33]
	v_mfma_f32_16x16x32_bf16 v[26:29], v[170:173], v[202:205], v[26:29]
	s_setprio 0
	s_setprio 1
	v_mfma_f32_16x16x32_bf16 v[66:69], v[142:145], v[174:177], v[66:69]
	v_mfma_f32_16x16x32_bf16 v[54:57], v[150:153], v[174:177], v[54:57]
	v_mfma_f32_16x16x32_bf16 v[50:53], v[142:145], v[182:185], v[50:53]
	v_mfma_f32_16x16x32_bf16 v[38:41], v[150:153], v[182:185], v[38:41]
	v_mfma_f32_16x16x32_bf16 v[34:37], v[142:145], v[190:193], v[34:37]
	v_mfma_f32_16x16x32_bf16 v[22:25], v[150:153], v[190:193], v[22:25]
	v_mfma_f32_16x16x32_bf16 v[18:21], v[142:145], v[198:201], v[18:21]
	v_mfma_f32_16x16x32_bf16 v[14:17], v[150:153], v[198:201], v[14:17]
	v_mfma_f32_16x16x32_bf16 v[66:69], v[146:149], v[178:181], v[66:69]
	v_mfma_f32_16x16x32_bf16 v[54:57], v[154:157], v[178:181], v[54:57]
	v_mfma_f32_16x16x32_bf16 v[50:53], v[146:149], v[186:189], v[50:53]
	v_mfma_f32_16x16x32_bf16 v[38:41], v[154:157], v[186:189], v[38:41]
	v_mfma_f32_16x16x32_bf16 v[34:37], v[146:149], v[194:197], v[34:37]
	v_mfma_f32_16x16x32_bf16 v[22:25], v[154:157], v[194:197], v[22:25]
	v_mfma_f32_16x16x32_bf16 v[18:21], v[146:149], v[202:205], v[18:21]
	v_mfma_f32_16x16x32_bf16 v[14:17], v[154:157], v[202:205], v[14:17]
	s_setprio 0
	s_barrier
	v_add_u32_e32 v2, 0x18000, v1
	ds_read_b128 v[158:161], v2
	ds_read_b128 v[162:165], v2 offset:1024
	ds_read_b128 v[166:169], v2 offset:2048
	ds_read_b128 v[170:173], v2 offset:3072
	v_add_u32_e32 v2, 0x1c000, v1
	ds_read_b128 v[142:145], v2
	ds_read_b128 v[146:149], v2 offset:1024
	ds_read_b128 v[150:153], v2 offset:2048
	ds_read_b128 v[154:157], v2 offset:3072
	s_add_u32 s4, s4, 0x80000
	s_addc_u32 s5, s5, 0
	s_mov_b32 m0, s44
	v_lshl_add_u64 v[232:233], s[4:5], 0, v[210:211]
	ds_read_b128 v[198:201], v230 offset:32768
	ds_read_b128 v[202:205], v230 offset:33792
	ds_read_b128 v[190:193], v230 offset:34816
	ds_read_b128 v[194:197], v230 offset:35840
	ds_read_b128 v[182:185], v230 offset:36864
	ds_read_b128 v[186:189], v230 offset:37888
	ds_read_b128 v[174:177], v230 offset:38912
	ds_read_b128 v[178:181], v230 offset:39936
	global_load_lds_dwordx4 v[232:233], off
	v_lshl_add_u64 v[232:233], s[4:5], 0, v[212:213]
	s_mov_b32 m0, s46
	s_nop 0
	global_load_lds_dwordx4 v[232:233], off
	s_cmp_eq_u32 s100, 3
	s_cbranch_scc1 .Lp4vg_w11_b1
	s_cmp_eq_u32 s100, 2
	s_cbranch_scc1 .Lp4vg_wk2_b1
	s_waitcnt vmcnt(8)
	s_branch .Lp4vg_wd_b1
